# diff-attention masked-step skip with every insertion padded to a multiple of 8 bytes (downstream code keeps its byte phase)
# baseline (speedup 1.0000x reference)
.LBB0_1365:
	s_and_b32 s72, s83, 0xffffffc0
	v_subrev_u32_e32 v130, s72, v219
	v_add_u32_e32 v182, 0x80, v130
	v_cvt_f32_i32_e32 v130, v182
	v_mul_f32_e64 v146, -v190, v130
	s_and_b32 s98, s65, 0xff
	s_cmp_gt_u32 s98, 0x60
	s_cbranch_scc1 .Lmk_a2
	v_mov_b32_e32 v221, 1.0
	v_mov_b32_e32 v222, 0
	v_mov_b32_e32 v223, 0
	v_readlane_b32 s76, v254, 14
	v_readlane_b32 s77, v254, 15
	v_readlane_b32 s83, v254, 16
	v_readlane_b32 s85, v254, 35
	s_mov_b32 s82, 0xf800000
	s_movk_i32 s84, 0x2200
	s_nop 4
	s_nop 0
	s_branch .Lmk_a2e

.LBB0_1371:
.Lmk_a2e:
	s_mul_i32 s3, s72, 0x3100
	s_sub_i32 s2, s72, 64
	s_add_i32 s7, s3, 0xfff3c000
	s_mul_hi_u32 s6, s2, 0x3100
	s_add_u32 s4, s80, s7
	s_addc_u32 s5, s81, s6
	v_lshl_add_u64 v[150:151], s[4:5], 0, v[194:195]
	s_sub_i32 s4, s72, 32
	s_add_i32 s3, s3, 0xfff9e000
	s_mul_hi_u32 s8, s4, 0x3100
	s_add_u32 s4, s80, s3
	s_addc_u32 s5, s81, s8
	v_lshl_add_u64 v[154:155], s[4:5], 0, v[194:195]
	s_add_u32 s4, s78, s7
	s_addc_u32 s5, s79, s6
	v_lshl_add_u64 v[182:183], s[4:5], 0, v[194:195]
	s_add_u32 s4, s78, s3
	global_load_dwordx4 v[146:149], v[150:151], off
	s_nop 0
	global_load_dwordx4 v[150:153], v[150:151], off offset:256
	s_nop 0
	global_load_dwordx4 v[158:161], v[154:155], off
	s_nop 0
	global_load_dwordx4 v[154:157], v[154:155], off offset:256
	s_addc_u32 s5, s79, s8
	v_lshl_add_u64 v[186:187], s[4:5], 0, v[194:195]
	global_load_dwordx4 v[182:185], v[182:183], off
	s_nop 0
	global_load_dwordx4 v[186:189], v[186:187], off
	s_nop 0
	s_cmp_le_u32 s98, 0x60
	s_cbranch_scc1 .Lmk_b2e
	s_setprio 1
	ds_read_b64_tr_b16 v[206:207], v213 offset:0
	ds_read_b64_tr_b16 v[208:209], v213 offset:0x1000
	ds_read_b64_tr_b16 v[238:239], v213 offset:0x2000
	ds_read_b64_tr_b16 v[240:241], v213 offset:0x3000
	ds_read_b64_tr_b16 v[244:245], v213 offset:0x4000
	ds_read_b64_tr_b16 v[246:247], v213 offset:0x5000
	ds_read_b64_tr_b16 v[250:251], v213 offset:0x6000
	ds_read_b64_tr_b16 v[252:253], v213 offset:0x7000
	s_waitcnt lgkmcnt(0)
	s_nop 0
	v_mfma_f32_32x32x16_bf16 v[114:129], v[130:133], v[206:209], v[114:129]
	ds_read_b64_tr_b16 v[206:207], v213 offset:0x200
	ds_read_b64_tr_b16 v[208:209], v213 offset:0x1200
	v_mfma_f32_32x32x16_bf16 v[114:129], v[134:137], v[238:241], v[114:129]
	ds_read_b64_tr_b16 v[238:239], v213 offset:0x2200
	ds_read_b64_tr_b16 v[240:241], v213 offset:0x3200
	v_mfma_f32_32x32x16_bf16 v[114:129], v[138:141], v[244:247], v[114:129]
	ds_read_b64_tr_b16 v[244:245], v213 offset:0x4200
	ds_read_b64_tr_b16 v[246:247], v213 offset:0x5200
	v_mfma_f32_32x32x16_bf16 v[114:129], v[142:145], v[250:253], v[114:129]
	ds_read_b64_tr_b16 v[250:251], v213 offset:0x6200
	ds_read_b64_tr_b16 v[252:253], v213 offset:0x7200
	s_waitcnt lgkmcnt(0)
	v_mfma_f32_32x32x16_bf16 v[98:113], v[130:133], v[206:209], v[98:113]
	ds_read_b64_tr_b16 v[206:207], v213 offset:0x400
	ds_read_b64_tr_b16 v[208:209], v213 offset:0x1400
	v_mfma_f32_32x32x16_bf16 v[98:113], v[134:137], v[238:241], v[98:113]
	ds_read_b64_tr_b16 v[238:239], v213 offset:0x2400
	ds_read_b64_tr_b16 v[240:241], v213 offset:0x3400
	v_mfma_f32_32x32x16_bf16 v[98:113], v[138:141], v[244:247], v[98:113]
	ds_read_b64_tr_b16 v[244:245], v213 offset:0x4400
	ds_read_b64_tr_b16 v[246:247], v213 offset:0x5400
	v_mfma_f32_32x32x16_bf16 v[98:113], v[142:145], v[250:253], v[98:113]
	ds_read_b64_tr_b16 v[250:251], v213 offset:0x6400
	ds_read_b64_tr_b16 v[252:253], v213 offset:0x7400
	s_waitcnt lgkmcnt(0)
	v_mfma_f32_32x32x16_bf16 v[82:97], v[130:133], v[206:209], v[82:97]
	ds_read_b64_tr_b16 v[206:207], v213 offset:0x600
	ds_read_b64_tr_b16 v[208:209], v213 offset:0x1600
	v_mfma_f32_32x32x16_bf16 v[82:97], v[134:137], v[238:241], v[82:97]
	ds_read_b64_tr_b16 v[238:239], v213 offset:0x2600
	ds_read_b64_tr_b16 v[240:241], v213 offset:0x3600
	v_mfma_f32_32x32x16_bf16 v[82:97], v[138:141], v[244:247], v[82:97]
	ds_read_b64_tr_b16 v[244:245], v213 offset:0x4600
	ds_read_b64_tr_b16 v[246:247], v213 offset:0x5600
	v_mfma_f32_32x32x16_bf16 v[82:97], v[142:145], v[250:253], v[82:97]
	ds_read_b64_tr_b16 v[250:251], v213 offset:0x6600
	ds_read_b64_tr_b16 v[252:253], v213 offset:0x7600
	s_waitcnt lgkmcnt(0)
	v_mfma_f32_32x32x16_bf16 v[66:81], v[130:133], v[206:209], v[66:81]
	ds_read_b64_tr_b16 v[206:207], v213 offset:0x800
	ds_read_b64_tr_b16 v[208:209], v213 offset:0x1800
	v_mfma_f32_32x32x16_bf16 v[66:81], v[134:137], v[238:241], v[66:81]
	ds_read_b64_tr_b16 v[238:239], v213 offset:0x2800
	ds_read_b64_tr_b16 v[240:241], v213 offset:0x3800
	v_mfma_f32_32x32x16_bf16 v[66:81], v[138:141], v[244:247], v[66:81]
	ds_read_b64_tr_b16 v[244:245], v213 offset:0x4800
	ds_read_b64_tr_b16 v[246:247], v213 offset:0x5800
	v_mfma_f32_32x32x16_bf16 v[66:81], v[142:145], v[250:253], v[66:81]
	ds_read_b64_tr_b16 v[250:251], v213 offset:0x6800
	ds_read_b64_tr_b16 v[252:253], v213 offset:0x7800
	s_waitcnt lgkmcnt(0)
	v_mfma_f32_32x32x16_bf16 v[50:65], v[130:133], v[206:209], v[50:65]
	ds_read_b64_tr_b16 v[206:207], v213 offset:0xa00
	ds_read_b64_tr_b16 v[208:209], v213 offset:0x1a00
	v_mfma_f32_32x32x16_bf16 v[50:65], v[134:137], v[238:241], v[50:65]
	ds_read_b64_tr_b16 v[238:239], v213 offset:0x2a00
	ds_read_b64_tr_b16 v[240:241], v213 offset:0x3a00
	v_mfma_f32_32x32x16_bf16 v[50:65], v[138:141], v[244:247], v[50:65]
	ds_read_b64_tr_b16 v[244:245], v213 offset:0x4a00
	ds_read_b64_tr_b16 v[246:247], v213 offset:0x5a00
	v_mfma_f32_32x32x16_bf16 v[50:65], v[142:145], v[250:253], v[50:65]
	ds_read_b64_tr_b16 v[250:251], v213 offset:0x6a00
	ds_read_b64_tr_b16 v[252:253], v213 offset:0x7a00
	s_waitcnt lgkmcnt(0)
	v_mfma_f32_32x32x16_bf16 v[34:49], v[130:133], v[206:209], v[34:49]
	ds_read_b64_tr_b16 v[206:207], v213 offset:0xc00
	ds_read_b64_tr_b16 v[208:209], v213 offset:0x1c00
	v_mfma_f32_32x32x16_bf16 v[34:49], v[134:137], v[238:241], v[34:49]
	ds_read_b64_tr_b16 v[238:239], v213 offset:0x2c00
	ds_read_b64_tr_b16 v[240:241], v213 offset:0x3c00
	v_mfma_f32_32x32x16_bf16 v[34:49], v[138:141], v[244:247], v[34:49]
	ds_read_b64_tr_b16 v[244:245], v213 offset:0x4c00
	ds_read_b64_tr_b16 v[246:247], v213 offset:0x5c00
	v_mfma_f32_32x32x16_bf16 v[34:49], v[142:145], v[250:253], v[34:49]
	ds_read_b64_tr_b16 v[250:251], v213 offset:0x6c00
	ds_read_b64_tr_b16 v[252:253], v213 offset:0x7c00
	s_waitcnt lgkmcnt(0)
	v_mfma_f32_32x32x16_bf16 v[18:33], v[130:133], v[206:209], v[18:33]
	ds_read_b64_tr_b16 v[206:207], v213 offset:0xe00
	ds_read_b64_tr_b16 v[208:209], v213 offset:0x1e00
	v_mfma_f32_32x32x16_bf16 v[18:33], v[134:137], v[238:241], v[18:33]
	ds_read_b64_tr_b16 v[238:239], v213 offset:0x2e00
	ds_read_b64_tr_b16 v[240:241], v213 offset:0x3e00
	v_mfma_f32_32x32x16_bf16 v[18:33], v[138:141], v[244:247], v[18:33]
	ds_read_b64_tr_b16 v[244:245], v213 offset:0x4e00
	ds_read_b64_tr_b16 v[246:247], v213 offset:0x5e00
	v_mfma_f32_32x32x16_bf16 v[18:33], v[142:145], v[250:253], v[18:33]
	ds_read_b64_tr_b16 v[250:251], v213 offset:0x6e00
	ds_read_b64_tr_b16 v[252:253], v213 offset:0x7e00
	s_waitcnt lgkmcnt(0)
	v_mfma_f32_32x32x16_bf16 v[2:17], v[130:133], v[206:209], v[2:17]
	v_mfma_f32_32x32x16_bf16 v[2:17], v[134:137], v[238:241], v[2:17]
	v_mfma_f32_32x32x16_bf16 v[2:17], v[138:141], v[244:247], v[2:17]
	v_mfma_f32_32x32x16_bf16 v[2:17], v[142:145], v[250:253], v[2:17]
	s_setprio 0

.LBB0_1377:
.Lmk_a1e:
	v_readlane_b32 s2, v254, 29
	v_readlane_b32 s3, v254, 30
	s_nop 1
	v_lshl_add_u64 v[130:131], s[2:3], 0, v[194:195]
	v_readlane_b32 s2, v254, 39
	v_add_co_u32_e32 v132, vcc, 0x62000, v130
	v_readlane_b32 s3, v254, 40
	s_nop 0
	v_addc_co_u32_e32 v133, vcc, 0, v131, vcc
	global_load_dwordx4 v[142:145], v[130:131], off
	global_load_dwordx4 v[146:149], v[130:131], off offset:256
	global_load_dwordx4 v[154:157], v[132:133], off
	global_load_dwordx4 v[150:153], v[132:133], off offset:256
	v_lshl_add_u64 v[130:131], s[2:3], 0, v[194:195]
	v_add_co_u32_e32 v132, vcc, 0x62000, v130
	s_nop 1
	v_addc_co_u32_e32 v133, vcc, 0, v131, vcc
	global_load_dwordx4 v[194:197], v[130:131], off
	global_load_dwordx4 v[198:201], v[132:133], off
	v_readlane_b32 s2, v254, 25
	v_readlane_b32 s3, v254, 26
	v_or_b32_e32 v132, s64, v242
	v_mov_b32_e32 v205, v1
	v_mov_b64_e32 v[130:131], s[2:3]
	v_mad_i64_i32 v[130:131], s[2:3], v132, s71, v[130:131]
	v_lshl_add_u64 v[138:139], v[130:131], 0, v[204:205]
	global_load_dwordx4 v[178:181], v[138:139], off
	global_load_dwordx4 v[170:173], v[138:139], off offset:32
	global_load_dwordx4 v[166:169], v[138:139], off offset:64
	global_load_dwordx4 v[162:165], v[138:139], off offset:96
	global_load_dwordx4 v[174:177], v[138:139], off offset:128
	global_load_dwordx4 v[130:133], v[138:139], off offset:160
	global_load_dwordx4 v[134:137], v[138:139], off offset:192
	s_nop 0
	global_load_dwordx4 v[138:141], v[138:139], off offset:224
	s_nop 0
	s_cmp_le_u32 s98, 0xa0
	s_cbranch_scc1 .Lmk_b1e
	s_setprio 1
	ds_read_b64_tr_b16 v[204:205], v213 offset:0x8000
	ds_read_b64_tr_b16 v[206:207], v213 offset:0x9000
	ds_read_b64_tr_b16 v[224:225], v213 offset:0xa000
	ds_read_b64_tr_b16 v[226:227], v213 offset:0xb000
	ds_read_b64_tr_b16 v[238:239], v213 offset:0xc000
	ds_read_b64_tr_b16 v[240:241], v213 offset:0xd000
	ds_read_b64_tr_b16 v[244:245], v213 offset:0xe000
	ds_read_b64_tr_b16 v[246:247], v213 offset:0xf000
	s_waitcnt lgkmcnt(0)
	s_nop 0
	v_mfma_f32_32x32x16_bf16 v[114:129], v[158:161], v[204:207], v[114:129]
	ds_read_b64_tr_b16 v[204:205], v213 offset:0x8200
	ds_read_b64_tr_b16 v[206:207], v213 offset:0x9200
	v_mfma_f32_32x32x16_bf16 v[114:129], v[182:185], v[224:227], v[114:129]
	ds_read_b64_tr_b16 v[224:225], v213 offset:0xa200
	ds_read_b64_tr_b16 v[226:227], v213 offset:0xb200
	v_mfma_f32_32x32x16_bf16 v[114:129], v[186:189], v[238:241], v[114:129]
	ds_read_b64_tr_b16 v[238:239], v213 offset:0xc200
	ds_read_b64_tr_b16 v[240:241], v213 offset:0xd200
	v_mfma_f32_32x32x16_bf16 v[114:129], v[190:193], v[244:247], v[114:129]
	ds_read_b64_tr_b16 v[244:245], v213 offset:0xe200
	ds_read_b64_tr_b16 v[246:247], v213 offset:0xf200
	s_waitcnt lgkmcnt(0)
	v_mfma_f32_32x32x16_bf16 v[98:113], v[158:161], v[204:207], v[98:113]
	ds_read_b64_tr_b16 v[204:205], v213 offset:0x8400
	ds_read_b64_tr_b16 v[206:207], v213 offset:0x9400
	v_mfma_f32_32x32x16_bf16 v[98:113], v[182:185], v[224:227], v[98:113]
	ds_read_b64_tr_b16 v[224:225], v213 offset:0xa400
	ds_read_b64_tr_b16 v[226:227], v213 offset:0xb400
	v_mfma_f32_32x32x16_bf16 v[98:113], v[186:189], v[238:241], v[98:113]
	ds_read_b64_tr_b16 v[238:239], v213 offset:0xc400
	ds_read_b64_tr_b16 v[240:241], v213 offset:0xd400
	v_mfma_f32_32x32x16_bf16 v[98:113], v[190:193], v[244:247], v[98:113]
	ds_read_b64_tr_b16 v[244:245], v213 offset:0xe400
	ds_read_b64_tr_b16 v[246:247], v213 offset:0xf400
	s_waitcnt lgkmcnt(0)
	v_mfma_f32_32x32x16_bf16 v[82:97], v[158:161], v[204:207], v[82:97]
	ds_read_b64_tr_b16 v[204:205], v213 offset:0x8600
	ds_read_b64_tr_b16 v[206:207], v213 offset:0x9600
	v_mfma_f32_32x32x16_bf16 v[82:97], v[182:185], v[224:227], v[82:97]
	ds_read_b64_tr_b16 v[224:225], v213 offset:0xa600
	ds_read_b64_tr_b16 v[226:227], v213 offset:0xb600
	v_mfma_f32_32x32x16_bf16 v[82:97], v[186:189], v[238:241], v[82:97]
	ds_read_b64_tr_b16 v[238:239], v213 offset:0xc600
	ds_read_b64_tr_b16 v[240:241], v213 offset:0xd600
	v_mfma_f32_32x32x16_bf16 v[82:97], v[190:193], v[244:247], v[82:97]
	ds_read_b64_tr_b16 v[244:245], v213 offset:0xe600
	ds_read_b64_tr_b16 v[246:247], v213 offset:0xf600
	s_waitcnt lgkmcnt(0)
	v_mfma_f32_32x32x16_bf16 v[66:81], v[158:161], v[204:207], v[66:81]
	ds_read_b64_tr_b16 v[204:205], v213 offset:0x8800
	ds_read_b64_tr_b16 v[206:207], v213 offset:0x9800
	v_mfma_f32_32x32x16_bf16 v[66:81], v[182:185], v[224:227], v[66:81]
	ds_read_b64_tr_b16 v[224:225], v213 offset:0xa800
	ds_read_b64_tr_b16 v[226:227], v213 offset:0xb800
	v_mfma_f32_32x32x16_bf16 v[66:81], v[186:189], v[238:241], v[66:81]
	ds_read_b64_tr_b16 v[238:239], v213 offset:0xc800
	ds_read_b64_tr_b16 v[240:241], v213 offset:0xd800
	v_mfma_f32_32x32x16_bf16 v[66:81], v[190:193], v[244:247], v[66:81]
	ds_read_b64_tr_b16 v[244:245], v213 offset:0xe800
	ds_read_b64_tr_b16 v[246:247], v213 offset:0xf800
	s_waitcnt lgkmcnt(0)
	v_mfma_f32_32x32x16_bf16 v[50:65], v[158:161], v[204:207], v[50:65]
	ds_read_b64_tr_b16 v[204:205], v213 offset:0x8a00
	ds_read_b64_tr_b16 v[206:207], v213 offset:0x9a00
	v_mfma_f32_32x32x16_bf16 v[50:65], v[182:185], v[224:227], v[50:65]
	ds_read_b64_tr_b16 v[224:225], v213 offset:0xaa00
	ds_read_b64_tr_b16 v[226:227], v213 offset:0xba00
	v_mfma_f32_32x32x16_bf16 v[50:65], v[186:189], v[238:241], v[50:65]
	ds_read_b64_tr_b16 v[238:239], v213 offset:0xca00
	ds_read_b64_tr_b16 v[240:241], v213 offset:0xda00
	v_mfma_f32_32x32x16_bf16 v[50:65], v[190:193], v[244:247], v[50:65]
	ds_read_b64_tr_b16 v[244:245], v213 offset:0xea00
	ds_read_b64_tr_b16 v[246:247], v213 offset:0xfa00
	s_waitcnt lgkmcnt(0)
	v_mfma_f32_32x32x16_bf16 v[34:49], v[158:161], v[204:207], v[34:49]
	ds_read_b64_tr_b16 v[204:205], v213 offset:0x8c00
	ds_read_b64_tr_b16 v[206:207], v213 offset:0x9c00
	v_mfma_f32_32x32x16_bf16 v[34:49], v[182:185], v[224:227], v[34:49]
	ds_read_b64_tr_b16 v[224:225], v213 offset:0xac00
	ds_read_b64_tr_b16 v[226:227], v213 offset:0xbc00
	v_mfma_f32_32x32x16_bf16 v[34:49], v[186:189], v[238:241], v[34:49]
	ds_read_b64_tr_b16 v[238:239], v213 offset:0xcc00
	ds_read_b64_tr_b16 v[240:241], v213 offset:0xdc00
	v_mfma_f32_32x32x16_bf16 v[34:49], v[190:193], v[244:247], v[34:49]
	ds_read_b64_tr_b16 v[244:245], v213 offset:0xec00
	ds_read_b64_tr_b16 v[246:247], v213 offset:0xfc00
	s_waitcnt lgkmcnt(0)
	v_mfma_f32_32x32x16_bf16 v[18:33], v[158:161], v[204:207], v[18:33]
	ds_read_b64_tr_b16 v[204:205], v213 offset:0x8e00
	ds_read_b64_tr_b16 v[206:207], v213 offset:0x9e00
	v_mfma_f32_32x32x16_bf16 v[18:33], v[182:185], v[224:227], v[18:33]
	ds_read_b64_tr_b16 v[224:225], v213 offset:0xae00
	ds_read_b64_tr_b16 v[226:227], v213 offset:0xbe00
	v_mfma_f32_32x32x16_bf16 v[18:33], v[186:189], v[238:241], v[18:33]
	ds_read_b64_tr_b16 v[238:239], v213 offset:0xce00
	ds_read_b64_tr_b16 v[240:241], v213 offset:0xde00
	v_mfma_f32_32x32x16_bf16 v[18:33], v[190:193], v[244:247], v[18:33]
	ds_read_b64_tr_b16 v[244:245], v213 offset:0xee00
	ds_read_b64_tr_b16 v[246:247], v213 offset:0xfe00
	s_waitcnt lgkmcnt(0)
	v_mfma_f32_32x32x16_bf16 v[2:17], v[158:161], v[204:207], v[2:17]
	v_mfma_f32_32x32x16_bf16 v[2:17], v[182:185], v[224:227], v[2:17]
	v_mfma_f32_32x32x16_bf16 v[2:17], v[186:189], v[238:241], v[2:17]
	v_mfma_f32_32x32x16_bf16 v[2:17], v[190:193], v[244:247], v[2:17]
	s_setprio 0
